# nt cache hint on once-read streaming loads: phase 7 residual x, phase 12 x1, phase 4 attention-output and conv inputs; on top of v46
# baseline (speedup 1.0000x reference)
; #define GAS __attribute__((address_space(1)))
; __device__ __forceinline__ int fresh_lane() { int l; asm volatile("v_mbcnt_lo_u32_b32 %0, -1, 0\n\tv_mbcnt_hi_u32_b32 %0, -1, %0" : "=v"(l)); return l; }
; __device__ __forceinline__ float dot4(f32x4 a, f32x4 b) { return (a.x * b.x + a.y * b.y) + (a.z * b.z + a.w * b.w); }
; __device__ __forceinline__ u32x2 pack4(f32x4 v) { u32x2 w; w.x = pk2(v.x, v.y); w.y = pk2(v.z, v.w); return w; }
; __device__ __forceinline__ f32x4 unpack4(u32x2 w) { return (f32x4){bflo(w.x), bfhi(w.x), bflo(w.y), bfhi(w.y)}; }
; __device__ __forceinline__ void phase4(KP kp, int wave, int bid, int G) {
;     const int lane = fresh_lane();
;     unsigned char* ws = KWS();
;     const int gw = bid * NWAVES + wave, NGW = G * NWAVES;
;     float lam;
;     { const float* q1 = (const float*)KIN(8); const float* k1 = (const float*)KIN(9); const float* q2 = (const float*)KIN(10); const float* k2 = (const float*)KIN(11);
;       const float s1 = wave_sum(q1[lane] * k1[lane] + q1[lane + 64] * k1[lane + 64]), s2 = wave_sum(q2[lane] * k2[lane] + q2[lane + 64] * k2[lane + 64]);
;       lam = expf(s1) - expf(s2) + 0.2f; }
;     const bf16* OA = (const bf16*)(ws + WS_OA); bf16* ON = (bf16*)(ws + WS_ON);
;     const f32x4 sg = *(const GAS f32x4*)((const float*)KIN(12) + 4 * lane) * 0.8f;
;     for (int it = gw; it < T * 8; it += NGW) { const int t = it >> 3, hd = it & 7;
;         const bf16* o0 = OA + (size_t)t * 4096 + hd * 512 + 4 * lane;
;         const f32x4 d = unpack4(*(const GAS u32x2*)o0) - lam * unpack4(*(const GAS u32x2*)(o0 + 256));
;         const float rstd = 1.0f / sqrtf(wave_sum(dot4(d, d)) * (1.0f / 256.0f) + EPS);
;         *(GAS u32x2*)(ON + (size_t)t * 4096 + hd * 256 + 4 * lane) = pack4(d * rstd * sg); }
.LBB0_706:
	s_cmp_lt_i32 s84, 5
	s_cselect_b64 s[2:3], -1, 0
	s_cmp_gt_i32 s85, 4
	s_cselect_b64 s[4:5], -1, 0
	s_and_b64 s[2:3], s[2:3], s[4:5]
	s_andn2_b64 vcc, exec, s[2:3]
	s_cbranch_vccnz .LBB0_767
	s_waitcnt lgkmcnt(0)
	s_mov_b64 s[26:27], s[0:1]
	s_waitcnt vmcnt(0)
	v_mbcnt_lo_u32_b32 v0, -1, 0
	v_mbcnt_hi_u32_b32 v0, -1, v0
	s_load_dwordx8 s[8:15], s[26:27], 0x40
	v_ashrrev_i32_e32 v1, 31, v0
	v_lshlrev_b64 v[2:3], 2, v[0:1]
	v_mbcnt_lo_u32_b32 v1, -1, 0
	s_lshl_b32 s2, s81, 3
	s_waitcnt lgkmcnt(0)
	v_lshl_add_u64 v[4:5], s[8:9], 0, v[2:3]
	v_lshl_add_u64 v[6:7], s[10:11], 0, v[2:3]
	global_load_dword v8, v[4:5], off
	global_load_dword v9, v[4:5], off offset:256
	global_load_dword v10, v[6:7], off
	global_load_dword v11, v[6:7], off offset:256
	v_lshl_add_u64 v[4:5], s[12:13], 0, v[2:3]
	v_lshl_add_u64 v[2:3], s[14:15], 0, v[2:3]
	global_load_dword v6, v[2:3], off offset:256
	global_load_dword v7, v[4:5], off offset:256
	global_load_dword v12, v[4:5], off
	global_load_dword v13, v[2:3], off
	v_mbcnt_hi_u32_b32 v3, -1, v1
	v_and_b32_e32 v1, 64, v3
	v_xor_b32_e32 v2, 1, v3
	v_add_u32_e32 v20, 64, v1
	v_cmp_lt_i32_e32 vcc, v2, v20
	v_xor_b32_e32 v4, 2, v3
	v_xor_b32_e32 v5, 4, v3
	v_cndmask_b32_e32 v1, v3, v2, vcc
	v_lshlrev_b32_e32 v1, 2, v1
	v_cmp_lt_i32_e32 vcc, v4, v20
	v_xor_b32_e32 v14, 8, v3
	v_xor_b32_e32 v15, 16, v3
	v_cndmask_b32_e32 v2, v3, v4, vcc
	v_lshlrev_b32_e32 v2, 2, v2
	v_cmp_lt_i32_e32 vcc, v5, v20
	v_xor_b32_e32 v19, 32, v3
	s_load_dwordx2 s[6:7], s[26:27], 0xc8
	v_cndmask_b32_e32 v5, v3, v5, vcc
	v_lshlrev_b32_e32 v16, 2, v5
	v_cmp_lt_i32_e32 vcc, v14, v20
	s_add_i32 s17, s82, s2
	s_lshl_b32 s18, s16, 3
	s_cmp_gt_i32 s17, 0xffff
	s_waitcnt vmcnt(4)
	v_mul_f32_e32 v9, v9, v11
	s_waitcnt vmcnt(2)
	v_mul_f32_e32 v6, v7, v6
	v_fmac_f32_e32 v9, v8, v10
	s_waitcnt vmcnt(0)
	v_fmac_f32_e32 v6, v12, v13
	ds_bpermute_b32 v7, v1, v9
	ds_bpermute_b32 v8, v1, v6
	s_waitcnt lgkmcnt(0)
	v_add_f32_e32 v4, v9, v7
	v_add_f32_e32 v6, v6, v8
	ds_bpermute_b32 v7, v2, v4
	ds_bpermute_b32 v8, v2, v6
	s_waitcnt lgkmcnt(1)
	v_add_f32_e32 v4, v4, v7
	s_waitcnt lgkmcnt(0)
	v_add_f32_e32 v5, v6, v8
	ds_bpermute_b32 v6, v16, v4
	ds_bpermute_b32 v7, v16, v5
	v_cndmask_b32_e32 v8, v3, v14, vcc
	v_lshlrev_b32_e32 v17, 2, v8
	v_cmp_lt_i32_e32 vcc, v15, v20
	s_waitcnt lgkmcnt(1)
	v_add_f32_e32 v4, v4, v6
	s_waitcnt lgkmcnt(0)
	v_add_f32_e32 v5, v5, v7
	ds_bpermute_b32 v6, v17, v4
	ds_bpermute_b32 v7, v17, v5
	v_cndmask_b32_e32 v8, v3, v15, vcc
	v_lshlrev_b32_e32 v18, 2, v8
	v_cmp_lt_i32_e32 vcc, v19, v20
	s_waitcnt lgkmcnt(1)
	v_add_f32_e32 v4, v4, v6
	s_waitcnt lgkmcnt(0)
	v_add_f32_e32 v6, v5, v7
	ds_bpermute_b32 v5, v18, v4
	ds_bpermute_b32 v7, v18, v6
	v_cndmask_b32_e32 v3, v3, v19, vcc
	v_lshlrev_b32_e32 v19, 2, v3
	s_waitcnt lgkmcnt(1)
	v_add_f32_e32 v5, v4, v5
	s_waitcnt lgkmcnt(0)
	v_add_f32_e32 v3, v6, v7
	ds_bpermute_b32 v6, v19, v5
	ds_bpermute_b32 v4, v19, v3
	s_cbranch_scc1 .LBB0_710
	s_load_dwordx2 s[2:3], s[26:27], 0x60
	v_lshlrev_b32_e32 v8, 2, v0
	v_ashrrev_i32_e32 v9, 31, v8
	s_mov_b32 s9, 0x3fb8aa3b
	s_waitcnt lgkmcnt(0)
	v_add_f32_e32 v3, v3, v4
	v_mov_b32_e32 v10, s2
	v_mov_b32_e32 v11, s3
	v_lshl_add_u64 v[10:11], v[8:9], 2, v[10:11]
	global_load_dwordx4 v[22:25], v[10:11], off
	v_add_f32_e32 v10, v5, v6
	v_mul_f32_e32 v4, 0x3fb8aa3b, v10
	v_mul_f32_e32 v5, 0x3fb8aa3b, v3
	v_fma_f32 v12, v10, s9, -v4
	v_rndne_f32_e32 v13, v4
	v_fma_f32 v14, v3, s9, -v5
	v_rndne_f32_e32 v15, v5
	v_fmac_f32_e32 v12, 0x32a5705f, v10
	v_sub_f32_e32 v4, v4, v13
	v_fmac_f32_e32 v14, 0x32a5705f, v3
	v_sub_f32_e32 v5, v5, v15
	v_add_f32_e32 v12, v4, v12
	v_lshlrev_b64 v[6:7], 1, v[8:9]
	v_cvt_i32_f32_e32 v8, v13
	v_add_f32_e32 v13, v5, v14
	v_exp_f32_e32 v12, v12
	v_cvt_i32_f32_e32 v9, v15
	v_exp_f32_e32 v13, v13
	s_mov_b32 s19, 0xc2ce8ed0
	v_ldexp_f32 v8, v12, v8
	v_cmp_ngt_f32_e32 vcc, s19, v10
	s_bfe_u32 s3, s66, 0x30006
	s_mov_b32 s20, 0x42b17218
	v_ldexp_f32 v9, v13, v9
	v_cndmask_b32_e32 v8, 0, v8, vcc
	v_cmp_ngt_f32_e32 vcc, s19, v3
	v_mov_b32_e32 v11, 0x7f800000
	s_lshl_b32 s21, s3, 9
	s_lshl_b32 s3, s3, 10
	v_cndmask_b32_e32 v9, 0, v9, vcc
	v_cmp_nlt_f32_e32 vcc, s20, v10
	s_add_u32 s14, s6, s3
	s_addc_u32 s15, s7, 0
	v_cndmask_b32_e32 v8, v11, v8, vcc
	v_cmp_nlt_f32_e32 vcc, s20, v3
	v_lshl_add_u64 v[4:5], s[14:15], 0, v[6:7]
	s_add_u32 s14, s6, s21
	v_cndmask_b32_e32 v3, v11, v9, vcc
	v_sub_f32_e32 v3, v8, v3
	s_addc_u32 s15, s7, 0
	v_add_f32_e32 v8, 0x3e4ccccd, v3
	s_mov_b32 s2, 0x3f4ccccd
	s_mov_b64 s[10:11], 0x48000000
	s_mov_b64 s[12:13], 0x4c000000
	v_lshl_add_u64 v[6:7], s[14:15], 0, v[6:7]
	v_mov_b32_e32 v10, v8
	s_mov_b32 s4, 0xffff0000
	v_mov_b32_e32 v20, 0x3727c5ac
	s_mov_b32 s5, 0xf800000
	v_mov_b32_e32 v21, 0x260
	s_movk_i32 s8, 0x7fff
	v_lshl_add_u64 v[4:5], v[4:5], 0, s[10:11]
	v_lshl_add_u64 v[6:7], v[6:7], 0, s[12:13]
	v_mov_b32_e32 v9, v8
	v_mov_b32_e32 v3, v8
	v_xor_b32_e32 v10, 0x80000000, v10
	s_mov_b32 s9, s17
	s_waitcnt vmcnt(0)
	v_pk_mul_f32 v[12:13], v[24:25], s[2:3] op_sel_hi:[1,0]
	v_pk_mul_f32 v[14:15], v[22:23], s[2:3] op_sel_hi:[1,0]
	s_ashr_i32 s22, s9, 3
	s_ashr_i32 s23, s22, 31
	s_lshl_b64 s[22:23], s[22:23], 13
	v_lshl_add_u64 v[60:61], v[4:5], 0, s[22:23]
	global_load_dwordx2 v[56:57], v[60:61], off nt
	global_load_dwordx2 v[58:59], v[60:61], off offset:512 nt
	s_add_i32 s24, s9, s18
	s_min_i32 s24, s24, 0xffff
	s_ashr_i32 s22, s24, 3
	s_ashr_i32 s23, s22, 31
	s_lshl_b64 s[22:23], s[22:23], 13
	v_lshl_add_u64 v[60:61], v[4:5], 0, s[22:23]
	global_load_dwordx2 v[62:63], v[60:61], off nt
	global_load_dwordx2 v[64:65], v[60:61], off offset:512 nt
	s_waitcnt vmcnt(0)
; #define GAS __attribute__((address_space(1)))
; __device__ __forceinline__ float dot4(f32x4 a, f32x4 b) { return (a.x * b.x + a.y * b.y) + (a.z * b.z + a.w * b.w); }
; __device__ __forceinline__ u32x2 pack4(f32x4 v) { u32x2 w; w.x = pk2(v.x, v.y); w.y = pk2(v.z, v.w); return w; }
; __device__ __forceinline__ f32x4 unpack4(u32x2 w) { return (f32x4){bflo(w.x), bfhi(w.x), bflo(w.y), bfhi(w.y)}; }
; __device__ __forceinline__ void phase4(KP kp, int wave, int bid, int G) {
;     ...
;     for (int it = gw; it < T * 8; it += NGW) { const int t = it >> 3, hd = it & 7;
;         const bf16* o0 = OA + (size_t)t * 4096 + hd * 512 + 4 * lane;
;         const f32x4 d = unpack4(*(const GAS u32x2*)o0) - lam * unpack4(*(const GAS u32x2*)(o0 + 256));
;         const float rstd = 1.0f / sqrtf(wave_sum(dot4(d, d)) * (1.0f / 256.0f) + EPS);
;         *(GAS u32x2*)(ON + (size_t)t * 4096 + hd * 256 + 4 * lane) = pack4(d * rstd * sg); }
.LBB0_709:
	s_ashr_i32 s2, s9, 3
	s_ashr_i32 s3, s2, 31
	s_lshl_b64 s[2:3], s[2:3], 13
	v_xor_b32_e32 v11, 0x80000000, v3
	v_lshl_add_u64 v[22:23], v[6:7], 0, s[2:3]
	s_lshl_b32 s24, s18, 1
	s_add_i32 s24, s24, s9
	s_min_i32 s24, s24, 0xffff
	s_ashr_i32 s22, s24, 3
	s_ashr_i32 s23, s22, 31
	s_lshl_b64 s[22:23], s[22:23], 13
	v_lshl_add_u64 v[60:61], v[4:5], 0, s[22:23]
	s_add_i32 s9, s9, s18
	s_waitcnt vmcnt(4)
	v_lshlrev_b32_e32 v28, 16, v56
	v_and_b32_e32 v29, 0xffff0000, v56
	v_lshlrev_b32_e32 v24, 16, v57
	v_and_b32_e32 v25, 0xffff0000, v57
	v_lshlrev_b32_e32 v30, 16, v58
	v_and_b32_e32 v31, 0xffff0000, v58
	v_lshlrev_b32_e32 v26, 16, v59
	v_and_b32_e32 v27, 0xffff0000, v59
	global_load_dwordx2 v[56:57], v[60:61], off nt
	global_load_dwordx2 v[58:59], v[60:61], off offset:512 nt
	v_pk_fma_f32 v[28:29], v[8:9], v[30:31], v[28:29] neg_lo:[1,0,0] neg_hi:[1,0,0]
	v_pk_fma_f32 v[24:25], v[10:11], v[26:27], v[24:25]
	v_pk_mul_f32 v[30:31], v[28:29], v[28:29]
	v_pk_mul_f32 v[26:27], v[24:25], v[24:25]
	s_nop 0
	v_pk_mov_b32 v[32:33], v[30:31], v[26:27] op_sel:[1,0]
	v_mov_b32_e32 v31, v27
	v_pk_add_f32 v[26:27], v[32:33], v[30:31]
	s_nop 0
	v_add_f32_e32 v11, v26, v27
	s_nop 1
	v_add_f32_dpp v11, v11, v11 quad_perm:[1,0,3,2] row_mask:0xf bank_mask:0xf
	s_nop 1
	v_add_f32_dpp v11, v11, v11 quad_perm:[2,3,0,1] row_mask:0xf bank_mask:0xf
	s_nop 1
	v_add_f32_dpp v11, v11, v11 row_half_mirror row_mask:0xf bank_mask:0xf
	s_nop 1
	v_add_f32_dpp v11, v11, v11 row_mirror row_mask:0xf bank_mask:0xf
	v_mov_b32_e32 v26, v11
	s_nop 1
	v_permlane16_swap_b32_e32 v11, v26
	v_add_f32_e32 v11, v11, v26
	v_mov_b32_e32 v26, v11
	s_nop 1
	v_permlane32_swap_b32_e32 v11, v26
	v_add_f32_e32 v11, v11, v26
	v_fmamk_f32 v11, v11, 0x3b800000, v20
	v_mul_f32_e32 v26, 0x4f800000, v11
	v_cmp_gt_f32_e32 vcc, s5, v11
	s_nop 1
	v_cndmask_b32_e32 v11, v11, v26, vcc
	v_sqrt_f32_e32 v26, v11
	s_nop 0
	v_add_u32_e32 v27, -1, v26
	v_add_u32_e32 v30, 1, v26
	v_fma_f32 v31, -v27, v26, v11
	v_fma_f32 v32, -v30, v26, v11
	v_cmp_ge_f32_e64 s[2:3], 0, v31
	s_nop 1
	v_cndmask_b32_e64 v26, v26, v27, s[2:3]
	v_cmp_lt_f32_e64 s[2:3], 0, v32
	s_nop 1
	v_cndmask_b32_e64 v26, v26, v30, s[2:3]
	v_mul_f32_e32 v27, 0x37800000, v26
	v_cndmask_b32_e32 v26, v26, v27, vcc
	v_cmp_class_f32_e32 vcc, v11, v21
	s_nop 1
	v_cndmask_b32_e32 v11, v26, v11, vcc
	v_div_scale_f32 v26, s[2:3], v11, v11, 1.0
	v_rcp_f32_e32 v30, v26
	v_div_scale_f32 v27, vcc, 1.0, v11, 1.0
	v_fma_f32 v31, -v26, v30, 1.0
	v_fmac_f32_e32 v30, v31, v30
	v_mul_f32_e32 v31, v27, v30
	v_fma_f32 v32, -v26, v31, v27
	v_fmac_f32_e32 v31, v32, v30
	v_fma_f32 v26, -v26, v31, v27
	v_div_fmas_f32 v26, v26, v30, v31
	v_div_fixup_f32 v26, v26, v11, 1.0
	v_pk_mul_f32 v[28:29], v[28:29], v[26:27] op_sel_hi:[1,0]
	v_pk_mul_f32 v[24:25], v[24:25], v[26:27] op_sel_hi:[1,0]
	v_pk_mul_f32 v[26:27], v[14:15], v[28:29]
	v_pk_mul_f32 v[24:25], v[12:13], v[24:25]
	v_bfe_u32 v11, v26, 16, 1
	v_bfe_u32 v29, v24, 16, 1
	v_bfe_u32 v28, v27, 16, 1
	v_bfe_u32 v30, v25, 16, 1
	v_add3_u32 v11, v26, v11, s8
	v_add3_u32 v24, v24, v29, s8
	v_add3_u32 v26, v27, v28, s8
	v_add3_u32 v25, v25, v30, s8
	v_lshrrev_b32_e32 v11, 16, v11
	v_lshrrev_b32_e32 v27, 16, v24
	v_and_or_b32 v24, v26, s4, v11
	v_and_or_b32 v25, v25, s4, v27
	global_store_dwordx2 v[22:23], v[24:25], off
	s_cmp_gt_i32 s9, 0xffff
	s_cbranch_scc1 .Lp4_exit
	s_ashr_i32 s2, s9, 3
	s_ashr_i32 s3, s2, 31
	s_lshl_b64 s[2:3], s[2:3], 13
	v_xor_b32_e32 v11, 0x80000000, v3
	v_lshl_add_u64 v[22:23], v[6:7], 0, s[2:3]
	s_lshl_b32 s24, s18, 1
	s_add_i32 s24, s24, s9
	s_min_i32 s24, s24, 0xffff
	s_ashr_i32 s22, s24, 3
	s_ashr_i32 s23, s22, 31
	s_lshl_b64 s[22:23], s[22:23], 13
	v_lshl_add_u64 v[60:61], v[4:5], 0, s[22:23]
	s_add_i32 s9, s9, s18
	s_waitcnt vmcnt(4)
	v_lshlrev_b32_e32 v28, 16, v62
	v_and_b32_e32 v29, 0xffff0000, v62
	v_lshlrev_b32_e32 v24, 16, v63
	v_and_b32_e32 v25, 0xffff0000, v63
	v_lshlrev_b32_e32 v30, 16, v64
	v_and_b32_e32 v31, 0xffff0000, v64
	v_lshlrev_b32_e32 v26, 16, v65
	v_and_b32_e32 v27, 0xffff0000, v65
	global_load_dwordx2 v[62:63], v[60:61], off nt
	global_load_dwordx2 v[64:65], v[60:61], off offset:512 nt
	v_pk_fma_f32 v[28:29], v[8:9], v[30:31], v[28:29] neg_lo:[1,0,0] neg_hi:[1,0,0]
	v_pk_fma_f32 v[24:25], v[10:11], v[26:27], v[24:25]
	v_pk_mul_f32 v[30:31], v[28:29], v[28:29]
	v_pk_mul_f32 v[26:27], v[24:25], v[24:25]
	s_nop 0
	v_pk_mov_b32 v[32:33], v[30:31], v[26:27] op_sel:[1,0]
	v_mov_b32_e32 v31, v27
	v_pk_add_f32 v[26:27], v[32:33], v[30:31]
	s_nop 0
	v_add_f32_e32 v11, v26, v27
	s_nop 1
	v_add_f32_dpp v11, v11, v11 quad_perm:[1,0,3,2] row_mask:0xf bank_mask:0xf
	s_nop 1
	v_add_f32_dpp v11, v11, v11 quad_perm:[2,3,0,1] row_mask:0xf bank_mask:0xf
	s_nop 1
	v_add_f32_dpp v11, v11, v11 row_half_mirror row_mask:0xf bank_mask:0xf
	s_nop 1
	v_add_f32_dpp v11, v11, v11 row_mirror row_mask:0xf bank_mask:0xf
	v_mov_b32_e32 v26, v11
	s_nop 1
	v_permlane16_swap_b32_e32 v11, v26
	v_add_f32_e32 v11, v11, v26
	v_mov_b32_e32 v26, v11
	s_nop 1
	v_permlane32_swap_b32_e32 v11, v26
	v_add_f32_e32 v11, v11, v26
	v_fmamk_f32 v11, v11, 0x3b800000, v20
	v_mul_f32_e32 v26, 0x4f800000, v11
	v_cmp_gt_f32_e32 vcc, s5, v11
	s_nop 1
	v_cndmask_b32_e32 v11, v11, v26, vcc
	v_sqrt_f32_e32 v26, v11
	s_nop 0
	v_add_u32_e32 v27, -1, v26
	v_add_u32_e32 v30, 1, v26
	v_fma_f32 v31, -v27, v26, v11
	v_fma_f32 v32, -v30, v26, v11
	v_cmp_ge_f32_e64 s[2:3], 0, v31
	s_nop 1
	v_cndmask_b32_e64 v26, v26, v27, s[2:3]
	v_cmp_lt_f32_e64 s[2:3], 0, v32
	s_nop 1
	v_cndmask_b32_e64 v26, v26, v30, s[2:3]
	v_mul_f32_e32 v27, 0x37800000, v26
	v_cndmask_b32_e32 v26, v26, v27, vcc
	v_cmp_class_f32_e32 vcc, v11, v21
	s_nop 1
	v_cndmask_b32_e32 v11, v26, v11, vcc
	v_div_scale_f32 v26, s[2:3], v11, v11, 1.0
	v_rcp_f32_e32 v30, v26
	v_div_scale_f32 v27, vcc, 1.0, v11, 1.0
	v_fma_f32 v31, -v26, v30, 1.0
	v_fmac_f32_e32 v30, v31, v30
	v_mul_f32_e32 v31, v27, v30
	v_fma_f32 v32, -v26, v31, v27
	v_fmac_f32_e32 v31, v32, v30
	v_fma_f32 v26, -v26, v31, v27
	v_div_fmas_f32 v26, v26, v30, v31
	v_div_fixup_f32 v26, v26, v11, 1.0
	v_pk_mul_f32 v[28:29], v[28:29], v[26:27] op_sel_hi:[1,0]
	v_pk_mul_f32 v[24:25], v[24:25], v[26:27] op_sel_hi:[1,0]
	v_pk_mul_f32 v[26:27], v[14:15], v[28:29]
	v_pk_mul_f32 v[24:25], v[12:13], v[24:25]
	v_bfe_u32 v11, v26, 16, 1
	v_bfe_u32 v29, v24, 16, 1
	v_bfe_u32 v28, v27, 16, 1
	v_bfe_u32 v30, v25, 16, 1
	v_add3_u32 v11, v26, v11, s8
	v_add3_u32 v24, v24, v29, s8
	v_add3_u32 v26, v27, v28, s8
	v_add3_u32 v25, v25, v30, s8
	v_lshrrev_b32_e32 v11, 16, v11
	v_lshrrev_b32_e32 v27, 16, v24
	v_and_or_b32 v24, v26, s4, v11
	v_and_or_b32 v25, v25, s4, v27
	global_store_dwordx2 v[22:23], v[24:25], off
	s_cmp_gt_i32 s9, 0xffff
	s_cbranch_scc0 .LBB0_709

; #define GAS __attribute__((address_space(1)))
; __device__ __forceinline__ u32x2 pack4(f32x4 v) { u32x2 w; w.x = pk2(v.x, v.y); w.y = pk2(v.z, v.w); return w; }
; __device__ __forceinline__ f32x4 unpack4(u32x2 w) { return (f32x4){bflo(w.x), bfhi(w.x), bflo(w.y), bfhi(w.y)}; }
; __device__ __forceinline__ void phase4(KP kp, int wave, int bid, int G) {
;     ...
;         for (int i = 0; i < 16; ++i) { const int t = t0 + i; const bf16* r = R + (size_t)t * 10240 + ch;
;             const v4u b = *(const GAS v4u*)r, c = *(const GAS v4u*)(r + 2048), h = *(const GAS v4u*)(r + 4096);
;             const f32x4 ua = unpack4((u32x2){c.x, c.y}) * unpack4((u32x2){h.x, h.y}), ub = unpack4((u32x2){c.z, c.w}) * unpack4((u32x2){h.z, h.w});
;             const f32x4 ya = unpack4((u32x2){b.x, b.y}) * (w0a * u2a + w1a * u1a + w2a * ua), yb = unpack4((u32x2){b.z, b.w}) * (w0b * u2b + w1b * u1b + w2b * ub);
;             const u32x2 pa = pack4(ya), pb = pack4(yb);
;             *(GAS v4u*)(CV + (size_t)t * 4096 + ch) = (v4u){pa.x, pa.y, pb.x, pb.y};
;             u2a = u1a; u2b = u1b; u1a = ua; u1b = ub; }
.LBB0_715:
	s_waitcnt vmcnt(4)
	v_pk_mul_f32 v[32:33], v[8:9], v[32:33]
	v_lshl_add_u64 v[2:3], s[14:15], 0, v[46:47]
	v_pk_mul_f32 v[60:61], v[8:9], v[36:37]
	s_waitcnt vmcnt(2)
	v_pk_fma_f32 v[68:69], v[16:17], v[36:37], v[32:33]
	v_add_co_u32_e64 v36, s[2:3], s29, v2
	v_lshl_add_u64 v[48:49], s[26:27], 0, v[46:47]
	v_pk_mul_f32 v[34:35], v[10:11], v[34:35]
	v_addc_co_u32_e64 v37, s[2:3], 0, v3, s[2:3]
	v_pk_fma_f32 v[66:67], v[18:19], v[38:39], v[34:35]
	v_add_co_u32_e64 v34, s[2:3], s30, v48
	v_pk_mul_f32 v[28:29], v[4:5], v[28:29]
	s_nop 0
	v_addc_co_u32_e64 v35, s[2:3], 0, v49, s[2:3]
	v_add_co_u32_e64 v72, s[2:3], s31, v48
	v_pk_fma_f32 v[70:71], v[12:13], v[40:41], v[28:29]
	s_nop 0
	v_addc_co_u32_e64 v73, s[2:3], 0, v49, s[2:3]
	v_add_co_u32_e64 v28, s[2:3], s34, v2
	v_pk_mul_f32 v[30:31], v[6:7], v[30:31]
	s_nop 0
	v_addc_co_u32_e64 v29, s[2:3], 0, v3, s[2:3]
	v_pk_mul_f32 v[62:63], v[6:7], v[42:43]
	v_pk_fma_f32 v[42:43], v[14:15], v[42:43], v[30:31]
	v_add_co_u32_e64 v30, s[2:3], s35, v48
	v_add_co_u32_e32 v50, vcc, 0x3e000000, v48
	s_nop 0
	v_addc_co_u32_e64 v31, s[2:3], 0, v49, s[2:3]
	v_add_co_u32_e64 v32, s[2:3], s36, v48
	v_addc_co_u32_e32 v51, vcc, 0, v49, vcc
	s_nop 0
	v_addc_co_u32_e64 v33, s[2:3], 0, v49, s[2:3]
	v_add_co_u32_e64 v74, s[2:3], s37, v2
	v_add_co_u32_e32 v52, vcc, 0x3e001000, v48
	s_nop 0
	v_addc_co_u32_e64 v75, s[2:3], 0, v3, s[2:3]
	v_add_co_u32_e64 v76, s[2:3], s38, v48
	v_addc_co_u32_e32 v53, vcc, 0, v49, vcc
	s_nop 0
	v_addc_co_u32_e64 v77, s[2:3], 0, v49, s[2:3]
	v_add_co_u32_e64 v78, s[2:3], s39, v48
	v_add_co_u32_e32 v48, vcc, 0x3e002000, v48
	s_nop 0
	v_addc_co_u32_e64 v79, s[2:3], 0, v49, s[2:3]
	v_addc_co_u32_e32 v49, vcc, 0, v49, vcc
	v_pk_mul_f32 v[58:59], v[10:11], v[38:39]
	v_pk_mul_f32 v[64:65], v[4:5], v[40:41]
	global_load_dwordx4 v[160:163], v[50:51], off nt
	global_load_dwordx4 v[164:167], v[48:49], off nt
	global_load_dwordx4 v[168:171], v[52:53], off nt
	global_load_dwordx4 v[172:175], v[34:35], off nt
	global_load_dwordx4 v[176:179], v[72:73], off nt
	global_load_dwordx4 v[180:183], v[34:35], off offset:-4096 nt
	global_load_dwordx4 v[184:187], v[30:31], off nt
	global_load_dwordx4 v[188:191], v[32:33], off nt
	global_load_dwordx4 v[192:195], v[30:31], off offset:-4096 nt
	global_load_dwordx4 v[196:199], v[76:77], off nt
	global_load_dwordx4 v[200:203], v[78:79], off nt
	global_load_dwordx4 v[204:207], v[76:77], off offset:-4096 nt
	s_add_u32 s14, s14, 0x8000
	s_addc_u32 s15, s15, 0
	s_add_u32 s26, s26, 0x14000
	s_addc_u32 s27, s27, 0
	s_add_i32 s41, s41, -4
	v_add_co_u32_e32 v2, vcc, s40, v2
	s_cmp_eq_u32 s41, 0
	s_nop 0
	v_addc_co_u32_e32 v3, vcc, 0, v3, vcc
	s_waitcnt vmcnt(9)
	v_mov_b32_e32 v38, v160
	v_mov_b32_e32 v39, v161
	v_mov_b32_e32 v40, v162
	v_mov_b32_e32 v41, v163
	v_mov_b32_e32 v54, v164
	v_mov_b32_e32 v55, v165
	v_mov_b32_e32 v56, v166
	v_mov_b32_e32 v57, v167
	v_mov_b32_e32 v50, v168
	v_mov_b32_e32 v51, v169
	v_mov_b32_e32 v52, v170
	v_mov_b32_e32 v53, v171
	v_lshlrev_b32_e32 v48, 16, v38
	v_lshlrev_b32_e32 v86, 16, v54
	v_and_b32_e32 v87, 0xffff0000, v54
	v_lshlrev_b32_e32 v82, 16, v50
	v_and_b32_e32 v83, 0xffff0000, v50
	v_lshlrev_b32_e32 v50, 16, v51
	v_and_b32_e32 v51, 0xffff0000, v51
	v_lshlrev_b32_e32 v84, 16, v52
	v_and_b32_e32 v85, 0xffff0000, v52
	v_lshlrev_b32_e32 v52, 16, v53
	v_and_b32_e32 v53, 0xffff0000, v53
	v_lshlrev_b32_e32 v54, 16, v55
	v_and_b32_e32 v55, 0xffff0000, v55
	v_lshlrev_b32_e32 v88, 16, v56
	v_and_b32_e32 v89, 0xffff0000, v56
	v_lshlrev_b32_e32 v56, 16, v57
	v_and_b32_e32 v57, 0xffff0000, v57
	v_pk_mul_f32 v[50:51], v[50:51], v[54:55]
	v_pk_mul_f32 v[54:55], v[82:83], v[86:87]
	v_pk_mul_f32 v[52:53], v[52:53], v[56:57]
	v_pk_mul_f32 v[56:57], v[84:85], v[88:89]
	v_and_b32_e32 v49, 0xffff0000, v38
	v_lshlrev_b32_e32 v38, 16, v39
	v_and_b32_e32 v39, 0xffff0000, v39
	v_lshlrev_b32_e32 v80, 16, v40
	v_and_b32_e32 v81, 0xffff0000, v40
	v_lshlrev_b32_e32 v40, 16, v41
	v_and_b32_e32 v41, 0xffff0000, v41
	v_pk_fma_f32 v[68:69], v[24:25], v[54:55], v[68:69]
	v_pk_fma_f32 v[66:67], v[26:27], v[50:51], v[66:67]
	v_pk_fma_f32 v[70:71], v[20:21], v[56:57], v[70:71]
	v_pk_fma_f32 v[42:43], v[22:23], v[52:53], v[42:43]
	v_pk_mul_f32 v[38:39], v[66:67], v[38:39]
	v_pk_mul_f32 v[48:49], v[68:69], v[48:49]
	v_pk_mul_f32 v[40:41], v[42:43], v[40:41]
	v_pk_mul_f32 v[42:43], v[70:71], v[80:81]
	v_pk_fma_f32 v[58:59], v[18:19], v[50:51], v[58:59]
	v_pk_mul_f32 v[82:83], v[10:11], v[50:51]
	v_bfe_u32 v1, v48, 16, 1
	v_bfe_u32 v50, v38, 16, 1
	v_bfe_u32 v66, v42, 16, 1
	v_bfe_u32 v68, v40, 16, 1
	v_bfe_u32 v45, v49, 16, 1
	v_bfe_u32 v51, v39, 16, 1
	v_bfe_u32 v67, v43, 16, 1
	v_bfe_u32 v69, v41, 16, 1
	v_add3_u32 v1, v48, v1, s28
	v_add3_u32 v38, v38, v50, s28
	v_add3_u32 v42, v42, v66, s28
	v_add3_u32 v40, v40, v68, s28
	v_add3_u32 v45, v49, v45, s28
	v_add3_u32 v39, v39, v51, s28
	v_add3_u32 v43, v43, v67, s28
	v_add3_u32 v41, v41, v69, s28
	v_lshrrev_b32_e32 v1, 16, v1
	v_lshrrev_b32_e32 v48, 16, v38
	v_lshrrev_b32_e32 v42, 16, v42
	v_lshrrev_b32_e32 v49, 16, v40
	v_and_or_b32 v38, v45, s25, v1
	v_and_or_b32 v39, v39, s25, v48
	v_and_or_b32 v40, v43, s25, v42
	v_and_or_b32 v41, v41, s25, v49
	global_store_dwordx4 v[36:37], v[38:41], off
	s_nop 0
	v_pk_fma_f32 v[60:61], v[16:17], v[54:55], v[60:61]
	v_pk_fma_f32 v[62:63], v[14:15], v[52:53], v[62:63]
	v_pk_fma_f32 v[64:65], v[12:13], v[56:57], v[64:65]
	v_pk_mul_f32 v[54:55], v[8:9], v[54:55]
	v_pk_mul_f32 v[56:57], v[4:5], v[56:57]
	v_pk_mul_f32 v[52:53], v[6:7], v[52:53]
	s_waitcnt vmcnt(7)
; #define GAS __attribute__((address_space(1)))
; __device__ __forceinline__ u32x2 pack4(f32x4 v) { u32x2 w; w.x = pk2(v.x, v.y); w.y = pk2(v.z, v.w); return w; }
; __device__ __forceinline__ f32x4 unpack4(u32x2 w) { return (f32x4){bflo(w.x), bfhi(w.x), bflo(w.y), bfhi(w.y)}; }
; __device__ __forceinline__ void phase4(KP kp, int wave, int bid, int G) {
;     ...
;         for (int i = 0; i < 16; ++i) { const int t = t0 + i; const bf16* r = R + (size_t)t * 10240 + ch;
;             const v4u b = *(const GAS v4u*)r, c = *(const GAS v4u*)(r + 2048), h = *(const GAS v4u*)(r + 4096);
;             const f32x4 ua = unpack4((u32x2){c.x, c.y}) * unpack4((u32x2){h.x, h.y}), ub = unpack4((u32x2){c.z, c.w}) * unpack4((u32x2){h.z, h.w});
;             const f32x4 ya = unpack4((u32x2){b.x, b.y}) * (w0a * u2a + w1a * u1a + w2a * ua), yb = unpack4((u32x2){b.z, b.w}) * (w0b * u2b + w1b * u1b + w2b * ub);
;             const u32x2 pa = pack4(ya), pb = pack4(yb);
;             *(GAS v4u*)(CV + (size_t)t * 4096 + ch) = (v4u){pa.x, pa.y, pb.x, pb.y};
;             u2a = u1a; u2b = u1b; u1a = ua; u1b = ub; }
	v_mov_b32_e32 v36, v172
	v_mov_b32_e32 v37, v173
	v_mov_b32_e32 v38, v174
	v_mov_b32_e32 v39, v175
	v_mov_b32_e32 v40, v176
	v_mov_b32_e32 v41, v177
	v_mov_b32_e32 v42, v178
	v_mov_b32_e32 v43, v179
	v_mov_b32_e32 v48, v180
	v_mov_b32_e32 v49, v181
	v_mov_b32_e32 v50, v182
	v_mov_b32_e32 v51, v183
	v_lshlrev_b32_e32 v34, 16, v36
	v_and_b32_e32 v35, 0xffff0000, v36
	v_lshlrev_b32_e32 v36, 16, v37
	v_and_b32_e32 v37, 0xffff0000, v37
	v_lshlrev_b32_e32 v66, 16, v40
	v_and_b32_e32 v67, 0xffff0000, v40
	v_lshlrev_b32_e32 v40, 16, v41
	v_and_b32_e32 v41, 0xffff0000, v41
	v_lshlrev_b32_e32 v68, 16, v38
	v_and_b32_e32 v69, 0xffff0000, v38
	v_lshlrev_b32_e32 v38, 16, v39
	v_and_b32_e32 v39, 0xffff0000, v39
	v_lshlrev_b32_e32 v70, 16, v42
	v_and_b32_e32 v71, 0xffff0000, v42
	v_lshlrev_b32_e32 v42, 16, v43
	v_and_b32_e32 v43, 0xffff0000, v43
	v_pk_mul_f32 v[84:85], v[36:37], v[40:41]
	v_pk_mul_f32 v[66:67], v[34:35], v[66:67]
	v_pk_mul_f32 v[86:87], v[38:39], v[42:43]
	v_pk_mul_f32 v[68:69], v[68:69], v[70:71]
	v_lshlrev_b32_e32 v72, 16, v48
	v_and_b32_e32 v73, 0xffff0000, v48
	v_lshlrev_b32_e32 v48, 16, v49
	v_and_b32_e32 v49, 0xffff0000, v49
	v_lshlrev_b32_e32 v80, 16, v50
	v_and_b32_e32 v81, 0xffff0000, v50
	v_lshlrev_b32_e32 v50, 16, v51
	v_and_b32_e32 v51, 0xffff0000, v51
	v_pk_fma_f32 v[34:35], v[24:25], v[66:67], v[60:61]
	v_pk_fma_f32 v[36:37], v[26:27], v[84:85], v[58:59]
	v_pk_fma_f32 v[38:39], v[20:21], v[68:69], v[64:65]
	v_pk_fma_f32 v[40:41], v[22:23], v[86:87], v[62:63]
	v_pk_mul_f32 v[36:37], v[36:37], v[48:49]
	v_pk_mul_f32 v[34:35], v[34:35], v[72:73]
	v_pk_mul_f32 v[40:41], v[40:41], v[50:51]
	v_pk_mul_f32 v[38:39], v[38:39], v[80:81]
	v_bfe_u32 v1, v34, 16, 1
	v_bfe_u32 v45, v35, 16, 1
	v_bfe_u32 v48, v36, 16, 1
	v_bfe_u32 v49, v37, 16, 1
	v_bfe_u32 v50, v38, 16, 1
	v_bfe_u32 v51, v39, 16, 1
	v_bfe_u32 v58, v40, 16, 1
	v_bfe_u32 v59, v41, 16, 1
	v_add3_u32 v1, v34, v1, s28
	v_add3_u32 v34, v35, v45, s28
	v_add3_u32 v35, v36, v48, s28
	v_add3_u32 v36, v37, v49, s28
	v_add3_u32 v37, v38, v50, s28
	v_add3_u32 v38, v39, v51, s28
	v_add3_u32 v39, v40, v58, s28
	v_add3_u32 v40, v41, v59, s28
	v_lshrrev_b32_e32 v1, 16, v1
	v_lshrrev_b32_e32 v35, 16, v35
	v_lshrrev_b32_e32 v37, 16, v37
	v_lshrrev_b32_e32 v39, 16, v39
	v_and_or_b32 v34, v34, s25, v1
	v_and_or_b32 v35, v36, s25, v35
	v_and_or_b32 v36, v38, s25, v37
	v_and_or_b32 v37, v40, s25, v39
	global_store_dwordx4 v[28:29], v[34:37], off
	s_nop 0
	s_nop 0
	v_pk_fma_f32 v[42:43], v[18:19], v[84:85], v[82:83]
	v_pk_fma_f32 v[54:55], v[16:17], v[66:67], v[54:55]
	v_pk_fma_f32 v[52:53], v[14:15], v[86:87], v[52:53]
	v_pk_fma_f32 v[56:57], v[12:13], v[68:69], v[56:57]
	s_waitcnt vmcnt(5)
; #define GAS __attribute__((address_space(1)))
; __device__ __forceinline__ u32x2 pack4(f32x4 v) { u32x2 w; w.x = pk2(v.x, v.y); w.y = pk2(v.z, v.w); return w; }
; __device__ __forceinline__ f32x4 unpack4(u32x2 w) { return (f32x4){bflo(w.x), bfhi(w.x), bflo(w.y), bfhi(w.y)}; }
; __device__ __forceinline__ void phase4(KP kp, int wave, int bid, int G) {
;     ...
;         for (int i = 0; i < 16; ++i) { const int t = t0 + i; const bf16* r = R + (size_t)t * 10240 + ch;
;             const v4u b = *(const GAS v4u*)r, c = *(const GAS v4u*)(r + 2048), h = *(const GAS v4u*)(r + 4096);
;             const f32x4 ua = unpack4((u32x2){c.x, c.y}) * unpack4((u32x2){h.x, h.y}), ub = unpack4((u32x2){c.z, c.w}) * unpack4((u32x2){h.z, h.w});
;             const f32x4 ya = unpack4((u32x2){b.x, b.y}) * (w0a * u2a + w1a * u1a + w2a * ua), yb = unpack4((u32x2){b.z, b.w}) * (w0b * u2b + w1b * u1b + w2b * ub);
;             const u32x2 pa = pack4(ya), pb = pack4(yb);
;             *(GAS v4u*)(CV + (size_t)t * 4096 + ch) = (v4u){pa.x, pa.y, pb.x, pb.y};
;             u2a = u1a; u2b = u1b; u1a = ua; u1b = ub; }
;     }
	v_mov_b32_e32 v34, v184
	v_mov_b32_e32 v35, v185
	v_mov_b32_e32 v36, v186
	v_mov_b32_e32 v37, v187
	v_mov_b32_e32 v38, v188
	v_mov_b32_e32 v39, v189
	v_mov_b32_e32 v40, v190
	v_mov_b32_e32 v41, v191
	v_mov_b32_e32 v28, v192
	v_mov_b32_e32 v29, v193
	v_mov_b32_e32 v30, v194
	v_mov_b32_e32 v31, v195
	v_lshlrev_b32_e32 v32, 16, v34
	v_and_b32_e32 v33, 0xffff0000, v34
	v_lshlrev_b32_e32 v34, 16, v35
	v_and_b32_e32 v35, 0xffff0000, v35
	v_lshlrev_b32_e32 v48, 16, v38
	v_and_b32_e32 v49, 0xffff0000, v38
	v_lshlrev_b32_e32 v38, 16, v39
	v_and_b32_e32 v39, 0xffff0000, v39
	v_lshlrev_b32_e32 v50, 16, v36
	v_and_b32_e32 v51, 0xffff0000, v36
	v_lshlrev_b32_e32 v36, 16, v37
	v_and_b32_e32 v37, 0xffff0000, v37
	v_lshlrev_b32_e32 v58, 16, v40
	v_and_b32_e32 v59, 0xffff0000, v40
	v_lshlrev_b32_e32 v40, 16, v41
	v_and_b32_e32 v41, 0xffff0000, v41
	v_lshlrev_b32_e32 v60, 16, v28
	v_and_b32_e32 v61, 0xffff0000, v28
	v_lshlrev_b32_e32 v62, 16, v29
	v_and_b32_e32 v63, 0xffff0000, v29
	v_lshlrev_b32_e32 v64, 16, v30
	v_and_b32_e32 v65, 0xffff0000, v30
	v_lshlrev_b32_e32 v70, 16, v31
	v_and_b32_e32 v71, 0xffff0000, v31
	v_pk_mul_f32 v[34:35], v[34:35], v[38:39]
	v_pk_mul_f32 v[32:33], v[32:33], v[48:49]
	v_pk_mul_f32 v[30:31], v[36:37], v[40:41]
	v_pk_mul_f32 v[28:29], v[50:51], v[58:59]
	v_pk_fma_f32 v[36:37], v[24:25], v[32:33], v[54:55]
	v_pk_fma_f32 v[38:39], v[26:27], v[34:35], v[42:43]
	v_pk_fma_f32 v[40:41], v[20:21], v[28:29], v[56:57]
	v_pk_fma_f32 v[42:43], v[22:23], v[30:31], v[52:53]
	v_pk_mul_f32 v[38:39], v[38:39], v[62:63]
	v_pk_mul_f32 v[36:37], v[36:37], v[60:61]
	v_pk_mul_f32 v[42:43], v[42:43], v[70:71]
	v_pk_mul_f32 v[40:41], v[40:41], v[64:65]
	v_bfe_u32 v1, v36, 16, 1
	v_bfe_u32 v45, v37, 16, 1
	v_bfe_u32 v48, v38, 16, 1
	v_bfe_u32 v49, v39, 16, 1
	v_bfe_u32 v50, v40, 16, 1
	v_bfe_u32 v51, v41, 16, 1
	v_bfe_u32 v52, v42, 16, 1
	v_bfe_u32 v53, v43, 16, 1
	v_add3_u32 v1, v36, v1, s28
	v_add3_u32 v36, v37, v45, s28
	v_add3_u32 v37, v38, v48, s28
	v_add3_u32 v38, v39, v49, s28
	v_add3_u32 v39, v40, v50, s28
	v_add3_u32 v40, v41, v51, s28
	v_add3_u32 v41, v42, v52, s28
	v_add3_u32 v42, v43, v53, s28
	v_lshrrev_b32_e32 v1, 16, v1
	v_lshrrev_b32_e32 v37, 16, v37
	v_lshrrev_b32_e32 v39, 16, v39
	v_lshrrev_b32_e32 v41, 16, v41
	v_and_or_b32 v36, v36, s25, v1
	v_and_or_b32 v37, v38, s25, v37
	v_and_or_b32 v38, v40, s25, v39
	v_and_or_b32 v39, v42, s25, v41
	global_store_dwordx4 v[74:75], v[36:39], off
	s_nop 0
	v_pk_mul_f32 v[52:53], v[8:9], v[66:67]
	v_pk_mul_f32 v[54:55], v[10:11], v[84:85]
	v_pk_mul_f32 v[56:57], v[4:5], v[68:69]
	v_pk_mul_f32 v[58:59], v[6:7], v[86:87]
	v_pk_fma_f32 v[54:55], v[18:19], v[34:35], v[54:55]
	v_pk_fma_f32 v[52:53], v[16:17], v[32:33], v[52:53]
	v_pk_fma_f32 v[58:59], v[14:15], v[30:31], v[58:59]
	v_pk_fma_f32 v[56:57], v[12:13], v[28:29], v[56:57]
	s_waitcnt vmcnt(3)
	v_mov_b32_e32 v36, v196
	v_mov_b32_e32 v37, v197
	v_mov_b32_e32 v38, v198
	v_mov_b32_e32 v39, v199
	v_mov_b32_e32 v40, v200
	v_mov_b32_e32 v41, v201
	v_mov_b32_e32 v42, v202
	v_mov_b32_e32 v43, v203
	v_mov_b32_e32 v48, v204
	v_mov_b32_e32 v49, v205
	v_mov_b32_e32 v50, v206
	v_mov_b32_e32 v51, v207
	v_lshlrev_b32_e32 v60, 16, v36
	v_and_b32_e32 v61, 0xffff0000, v36
	v_lshlrev_b32_e32 v36, 16, v37
	v_and_b32_e32 v37, 0xffff0000, v37
	v_lshlrev_b32_e32 v62, 16, v40
	v_and_b32_e32 v63, 0xffff0000, v40
	v_lshlrev_b32_e32 v40, 16, v41
	v_and_b32_e32 v41, 0xffff0000, v41
	v_lshlrev_b32_e32 v64, 16, v38
	v_and_b32_e32 v65, 0xffff0000, v38
	v_lshlrev_b32_e32 v66, 16, v39
	v_and_b32_e32 v67, 0xffff0000, v39
	v_lshlrev_b32_e32 v68, 16, v42
	v_and_b32_e32 v69, 0xffff0000, v42
	v_lshlrev_b32_e32 v42, 16, v43
	v_and_b32_e32 v43, 0xffff0000, v43
	v_pk_mul_f32 v[38:39], v[36:37], v[40:41]
	v_pk_mul_f32 v[36:37], v[60:61], v[62:63]
	v_pk_mul_f32 v[42:43], v[66:67], v[42:43]
	v_pk_mul_f32 v[40:41], v[64:65], v[68:69]
	v_lshlrev_b32_e32 v70, 16, v48
	v_and_b32_e32 v71, 0xffff0000, v48
	v_lshlrev_b32_e32 v48, 16, v49
	v_and_b32_e32 v49, 0xffff0000, v49
	v_lshlrev_b32_e32 v72, 16, v50
	v_and_b32_e32 v73, 0xffff0000, v50
	v_lshlrev_b32_e32 v50, 16, v51
	v_and_b32_e32 v51, 0xffff0000, v51
	v_pk_fma_f32 v[52:53], v[24:25], v[36:37], v[52:53]
	v_pk_fma_f32 v[54:55], v[26:27], v[38:39], v[54:55]
	v_pk_fma_f32 v[56:57], v[20:21], v[40:41], v[56:57]
	v_pk_fma_f32 v[58:59], v[22:23], v[42:43], v[58:59]
	v_pk_mul_f32 v[48:49], v[54:55], v[48:49]
	v_pk_mul_f32 v[52:53], v[52:53], v[70:71]
	v_pk_mul_f32 v[50:51], v[58:59], v[50:51]
	v_pk_mul_f32 v[54:55], v[56:57], v[72:73]
	v_bfe_u32 v1, v52, 16, 1
	v_bfe_u32 v56, v48, 16, 1
	v_bfe_u32 v58, v54, 16, 1
	v_bfe_u32 v60, v50, 16, 1
	v_bfe_u32 v45, v53, 16, 1
	v_bfe_u32 v57, v49, 16, 1
	v_bfe_u32 v59, v55, 16, 1
	v_bfe_u32 v61, v51, 16, 1
	v_add3_u32 v1, v52, v1, s28
	v_add3_u32 v48, v48, v56, s28
	v_add3_u32 v52, v54, v58, s28
	v_add3_u32 v50, v50, v60, s28
	v_add3_u32 v45, v53, v45, s28
	v_add3_u32 v49, v49, v57, s28
	v_add3_u32 v53, v55, v59, s28
	v_add3_u32 v51, v51, v61, s28
	v_lshrrev_b32_e32 v1, 16, v1
	v_lshrrev_b32_e32 v54, 16, v48
	v_lshrrev_b32_e32 v52, 16, v52
	v_lshrrev_b32_e32 v55, 16, v50
	v_and_or_b32 v48, v45, s25, v1
	v_and_or_b32 v49, v49, s25, v54
	v_and_or_b32 v50, v53, s25, v52
	v_and_or_b32 v51, v51, s25, v55
	global_store_dwordx4 v[2:3], v[48:51], off
	s_cbranch_scc0 .LBB0_715
	s_add_i32 s17, s17, s18
	s_add_i32 s20, s20, s21
	s_add_i32 s22, s22, s23
	s_cmpk_gt_i32 s17, 0x7ff
	s_cbranch_scc0 .LBB0_712

; #define LAS __attribute__((address_space(3)))
; __device__ __forceinline__ int fresh_lane() { int l; asm volatile("v_mbcnt_lo_u32_b32 %0, -1, 0\n\tv_mbcnt_hi_u32_b32 %0, -1, %0" : "=v"(l)); return l; }
; __device__ __forceinline__ float half_max(float v) { v = fmaxf(v, __shfl_xor(v, 1)); v = fmaxf(v, __shfl_xor(v, 2)); v = fmaxf(v, __shfl_xor(v, 4)); v = fmaxf(v, __shfl_xor(v, 8)); v = fmaxf(v, __shfl_xor(v, 16)); return v; }
; __device__ __forceinline__ int half_min(int v) { v = min(v, __shfl_xor(v, 1)); v = min(v, __shfl_xor(v, 2)); v = min(v, __shfl_xor(v, 4)); v = min(v, __shfl_xor(v, 8)); v = min(v, __shfl_xor(v, 16)); return v; }
; __device__ __forceinline__ void phase8(KP kp, LAS unsigned char* lds, int wave, int bid) {
;     const int lane = fresh_lane(), tid = wave * 64 + lane;
;     unsigned char* ws = KWS();
;     LAS float* A2 = (LAS float*)lds; LAS float* B2 = A2 + 2048;
;     LAS float* rs = (LAS float*)(lds + 16384);
;     LAS int* eidx = (LAS int*)(lds + 16384 + 128);
;     LAS float* part = (LAS float*)(lds + 20480);
;     LAS float* lg = (LAS float*)(lds + 56320);
;     const float* mod = (const float*)(ws + WS_MOD); const float* n2g = (const float*)KIN(16);
;     for (int c = tid; c < 2048; c += 512) { A2[c] = n2g[c] * (1.0f + mod[4 * 2048 + c]); B2[c] = mod[3 * 2048 + c]; }
;     __syncthreads();
;     const float* X1 = (const float*)(ws + WS_X1); bf16* H = (bf16*)(ws + WS_H); const float* wrt = (const float*)(ws + WS_WRT); const float* br = (const float*)KIN(18);
;     int* TOPI = (int*)(ws + WS_TOPI); float* TOPW = (float*)(ws + WS_TOPW);
.LBB0_863:
	v_lshl_add_u32 v174, s46, 8, v164
	v_lshl_or_b32 v162, s5, 8, v166
	v_ashrrev_i32_e32 v175, 31, v174
	v_ashrrev_i32_e32 v163, 31, v162
	v_lshlrev_b64 v[130:131], 11, v[174:175]
	v_lshl_add_u64 v[130:131], v[130:131], 0, v[162:163]
	v_lshlrev_b64 v[160:161], 2, v[130:131]
	v_lshl_add_u64 v[128:129], v[162:163], 2, s[10:11]
	v_lshl_add_u64 v[176:177], s[2:3], 0, v[160:161]
	v_lshl_add_u64 v[158:159], s[8:9], 0, v[160:161]
	s_mov_b64 s[48:49], 0x20000
	s_mov_b64 s[50:51], 0x40000
	s_mov_b64 s[52:53], 0x60000
	global_load_dwordx4 v[140:143], v[128:129], off
	global_load_dwordx4 v[136:139], v[128:129], off offset:64
	global_load_dwordx4 v[132:135], v[128:129], off offset:512
	s_nop 0
	global_load_dwordx4 v[128:131], v[128:129], off offset:576
	global_load_dwordx4 v[178:181], v[176:177], off nt
	global_load_dwordx4 v[182:185], v[176:177], off offset:64 nt
	global_load_dwordx4 v[186:189], v[176:177], off offset:512 nt
	global_load_dwordx4 v[190:193], v[176:177], off offset:576 nt
	v_lshl_add_u64 v[170:171], v[176:177], 0, s[48:49]
	global_load_dwordx4 v[194:197], v[170:171], off nt
	global_load_dwordx4 v[198:201], v[170:171], off offset:64 nt
	global_load_dwordx4 v[202:205], v[170:171], off offset:512 nt
	global_load_dwordx4 v[206:209], v[170:171], off offset:576 nt
	v_lshl_add_u64 v[162:163], v[176:177], 0, s[50:51]
	global_load_dwordx4 v[210:213], v[162:163], off nt
	global_load_dwordx4 v[214:217], v[162:163], off offset:64 nt
	global_load_dwordx4 v[218:221], v[162:163], off offset:512 nt
	global_load_dwordx4 v[222:225], v[162:163], off offset:576 nt
	v_lshl_add_u64 v[170:171], v[176:177], 0, s[52:53]
	global_load_dwordx4 v[226:229], v[170:171], off nt
	global_load_dwordx4 v[230:233], v[170:171], off offset:64 nt
	global_load_dwordx4 v[234:237], v[170:171], off offset:512 nt
	global_load_dwordx4 v[238:241], v[170:171], off offset:576 nt
	s_waitcnt vmcnt(8)
	v_pk_fma_f32 v[126:127], v[126:127], v[142:143], v[180:181]
	v_pk_fma_f32 v[124:125], v[124:125], v[140:141], v[178:179]
	global_store_dwordx4 v[158:159], v[124:127], off
	v_pk_fma_f32 v[122:123], v[122:123], v[138:139], v[184:185]
	v_pk_fma_f32 v[120:121], v[120:121], v[136:137], v[182:183]
	global_store_dwordx4 v[158:159], v[120:123], off offset:64
	v_pk_fma_f32 v[118:119], v[118:119], v[134:135], v[188:189]
	v_pk_fma_f32 v[116:117], v[116:117], v[132:133], v[186:187]
	global_store_dwordx4 v[158:159], v[116:119], off offset:512
	v_pk_fma_f32 v[110:111], v[110:111], v[130:131], v[192:193]
	v_pk_fma_f32 v[108:109], v[108:109], v[128:129], v[190:191]
	global_store_dwordx4 v[158:159], v[108:111], off offset:576
	v_lshl_add_u64 v[174:175], v[158:159], 0, s[48:49]
	v_pk_fma_f32 v[114:115], v[114:115], v[142:143], v[196:197]
	v_pk_fma_f32 v[112:113], v[112:113], v[140:141], v[194:195]
	global_store_dwordx4 v[174:175], v[112:115], off
	v_pk_fma_f32 v[106:107], v[106:107], v[138:139], v[200:201]
	v_pk_fma_f32 v[104:105], v[104:105], v[136:137], v[198:199]
	global_store_dwordx4 v[174:175], v[104:107], off offset:64
	v_pk_fma_f32 v[102:103], v[102:103], v[134:135], v[204:205]
	v_pk_fma_f32 v[100:101], v[100:101], v[132:133], v[202:203]
	global_store_dwordx4 v[174:175], v[100:103], off offset:512
	v_pk_fma_f32 v[94:95], v[94:95], v[130:131], v[208:209]
	v_pk_fma_f32 v[92:93], v[92:93], v[128:129], v[206:207]
	global_store_dwordx4 v[174:175], v[92:95], off offset:576
	v_lshl_add_u64 v[162:163], v[176:177], 0, s[26:27]
	global_load_dwordx4 v[178:181], v[162:163], off nt
	global_load_dwordx4 v[182:185], v[162:163], off offset:64 nt
	global_load_dwordx4 v[186:189], v[162:163], off offset:512 nt
	global_load_dwordx4 v[190:193], v[162:163], off offset:576 nt
	v_lshl_add_u64 v[170:171], v[176:177], 0, s[28:29]
	global_load_dwordx4 v[194:197], v[170:171], off nt
	global_load_dwordx4 v[198:201], v[170:171], off offset:64 nt
	global_load_dwordx4 v[202:205], v[170:171], off offset:512 nt
	global_load_dwordx4 v[206:209], v[170:171], off offset:576 nt
	s_waitcnt vmcnt(16)
; #define LAS __attribute__((address_space(3)))
; __device__ __forceinline__ void phase8(KP kp, LAS unsigned char* lds, int wave, int bid) {
;     ...
;     LAS float* lg = (LAS float*)(lds + 56320);
;     const float* mod = (const float*)(ws + WS_MOD); const float* n2g = (const float*)KIN(16);
;     for (int c = tid; c < 2048; c += 512) { A2[c] = n2g[c] * (1.0f + mod[4 * 2048 + c]); B2[c] = mod[3 * 2048 + c]; }
;     __syncthreads();
;     const float* X1 = (const float*)(ws + WS_X1); bf16* H = (bf16*)(ws + WS_H); const float* wrt = (const float*)(ws + WS_WRT); const float* br = (const float*)KIN(18);
;     int* TOPI = (int*)(ws + WS_TOPI); float* TOPW = (float*)(ws + WS_TOPW);
	v_lshl_add_u64 v[172:173], v[158:159], 0, s[50:51]
	v_pk_fma_f32 v[98:99], v[98:99], v[142:143], v[212:213]
	v_pk_fma_f32 v[96:97], v[96:97], v[140:141], v[210:211]
	global_store_dwordx4 v[172:173], v[96:99], off
	v_pk_fma_f32 v[90:91], v[90:91], v[138:139], v[216:217]
	v_pk_fma_f32 v[88:89], v[88:89], v[136:137], v[214:215]
	global_store_dwordx4 v[172:173], v[88:91], off offset:64
	v_pk_fma_f32 v[86:87], v[86:87], v[134:135], v[220:221]
	v_pk_fma_f32 v[84:85], v[84:85], v[132:133], v[218:219]
	global_store_dwordx4 v[172:173], v[84:87], off offset:512
	v_pk_fma_f32 v[78:79], v[78:79], v[130:131], v[224:225]
	v_pk_fma_f32 v[76:77], v[76:77], v[128:129], v[222:223]
	global_store_dwordx4 v[172:173], v[76:79], off offset:576
	v_lshl_add_u64 v[174:175], v[158:159], 0, s[52:53]
	v_pk_fma_f32 v[82:83], v[82:83], v[142:143], v[228:229]
	v_pk_fma_f32 v[80:81], v[80:81], v[140:141], v[226:227]
	global_store_dwordx4 v[174:175], v[80:83], off
	v_pk_fma_f32 v[74:75], v[74:75], v[138:139], v[232:233]
	v_pk_fma_f32 v[72:73], v[72:73], v[136:137], v[230:231]
	global_store_dwordx4 v[174:175], v[72:75], off offset:64
	v_pk_fma_f32 v[70:71], v[70:71], v[134:135], v[236:237]
	v_pk_fma_f32 v[68:69], v[68:69], v[132:133], v[234:235]
	global_store_dwordx4 v[174:175], v[68:71], off offset:512
	v_pk_fma_f32 v[66:67], v[66:67], v[130:131], v[240:241]
	v_pk_fma_f32 v[64:65], v[64:65], v[128:129], v[238:239]
	global_store_dwordx4 v[174:175], v[64:67], off offset:576
	v_lshl_add_u64 v[162:163], v[176:177], 0, s[30:31]
	global_load_dwordx4 v[210:213], v[162:163], off nt
	global_load_dwordx4 v[214:217], v[162:163], off offset:64 nt
	global_load_dwordx4 v[218:221], v[162:163], off offset:512 nt
	global_load_dwordx4 v[222:225], v[162:163], off offset:576 nt
	v_lshl_add_u64 v[170:171], v[176:177], 0, s[34:35]
	global_load_dwordx4 v[226:229], v[170:171], off nt
	global_load_dwordx4 v[230:233], v[170:171], off offset:64 nt
	global_load_dwordx4 v[234:237], v[170:171], off offset:512 nt
	global_load_dwordx4 v[238:241], v[170:171], off offset:576 nt
	s_waitcnt vmcnt(16)
	v_lshl_add_u64 v[172:173], v[158:159], 0, s[26:27]
	v_pk_fma_f32 v[62:63], v[62:63], v[142:143], v[180:181]
	v_pk_fma_f32 v[60:61], v[60:61], v[140:141], v[178:179]
	global_store_dwordx4 v[172:173], v[60:63], off
	v_pk_fma_f32 v[58:59], v[58:59], v[138:139], v[184:185]
	v_pk_fma_f32 v[56:57], v[56:57], v[136:137], v[182:183]
	global_store_dwordx4 v[172:173], v[56:59], off offset:64
	v_pk_fma_f32 v[54:55], v[54:55], v[134:135], v[188:189]
	v_pk_fma_f32 v[52:53], v[52:53], v[132:133], v[186:187]
	global_store_dwordx4 v[172:173], v[52:55], off offset:512
	v_pk_fma_f32 v[46:47], v[46:47], v[130:131], v[192:193]
	v_pk_fma_f32 v[44:45], v[44:45], v[128:129], v[190:191]
	global_store_dwordx4 v[172:173], v[44:47], off offset:576
	v_lshl_add_u64 v[174:175], v[158:159], 0, s[28:29]
	v_pk_fma_f32 v[50:51], v[50:51], v[142:143], v[196:197]
	v_pk_fma_f32 v[48:49], v[48:49], v[140:141], v[194:195]
	global_store_dwordx4 v[174:175], v[48:51], off
	v_pk_fma_f32 v[42:43], v[42:43], v[138:139], v[200:201]
	v_pk_fma_f32 v[40:41], v[40:41], v[136:137], v[198:199]
	global_store_dwordx4 v[174:175], v[40:43], off offset:64
	v_pk_fma_f32 v[38:39], v[38:39], v[134:135], v[204:205]
	v_pk_fma_f32 v[36:37], v[36:37], v[132:133], v[202:203]
	global_store_dwordx4 v[174:175], v[36:39], off offset:512
	v_pk_fma_f32 v[30:31], v[30:31], v[130:131], v[208:209]
	v_pk_fma_f32 v[28:29], v[28:29], v[128:129], v[206:207]
	global_store_dwordx4 v[174:175], v[28:31], off offset:576
	s_waitcnt vmcnt(8)
	v_lshl_add_u64 v[172:173], v[158:159], 0, s[30:31]
	v_pk_fma_f32 v[34:35], v[34:35], v[142:143], v[212:213]
	v_pk_fma_f32 v[32:33], v[32:33], v[140:141], v[210:211]
	global_store_dwordx4 v[172:173], v[32:35], off
	v_pk_fma_f32 v[26:27], v[26:27], v[138:139], v[216:217]
	v_pk_fma_f32 v[24:25], v[24:25], v[136:137], v[214:215]
	global_store_dwordx4 v[172:173], v[24:27], off offset:64
	v_pk_fma_f32 v[22:23], v[22:23], v[134:135], v[220:221]
	v_pk_fma_f32 v[20:21], v[20:21], v[132:133], v[218:219]
	global_store_dwordx4 v[172:173], v[20:23], off offset:512
	v_pk_fma_f32 v[14:15], v[14:15], v[130:131], v[224:225]
	v_pk_fma_f32 v[12:13], v[12:13], v[128:129], v[222:223]
	global_store_dwordx4 v[172:173], v[12:15], off offset:576
	v_lshl_add_u64 v[174:175], v[158:159], 0, s[34:35]
	v_pk_fma_f32 v[18:19], v[18:19], v[142:143], v[228:229]
	v_pk_fma_f32 v[16:17], v[16:17], v[140:141], v[226:227]
	global_store_dwordx4 v[174:175], v[16:19], off
	v_pk_fma_f32 v[10:11], v[10:11], v[138:139], v[232:233]
	v_pk_fma_f32 v[8:9], v[8:9], v[136:137], v[230:231]
	global_store_dwordx4 v[174:175], v[8:11], off offset:64
	v_pk_fma_f32 v[6:7], v[6:7], v[134:135], v[236:237]
	v_pk_fma_f32 v[4:5], v[4:5], v[132:133], v[234:235]
	global_store_dwordx4 v[174:175], v[4:7], off offset:512
	v_pk_fma_f32 v[2:3], v[2:3], v[130:131], v[240:241]
	v_pk_fma_f32 v[0:1], v[0:1], v[128:129], v[238:239]
	global_store_dwordx4 v[174:175], v[0:3], off offset:576
	s_andn2_b64 vcc, exec, s[40:41]
	s_mov_b64 s[40:41], -1
	s_cbranch_vccnz .LBB0_851
	s_andn2_b64 vcc, exec, s[6:7]
	s_cbranch_vccnz .LBB0_850
	s_barrier
	s_branch .LBB0_850

; #define GAS __attribute__((address_space(1)))
; __device__ __forceinline__ float dot4(f32x4 a, f32x4 b) { return (a.x * b.x + a.y * b.y) + (a.z * b.z + a.w * b.w); }
; __device__ __forceinline__ f32x4 unpack4(u32x2 w) { return (f32x4){bflo(w.x), bfhi(w.x), bflo(w.y), bfhi(w.y)}; }
; __device__ __forceinline__ void phase12(KP kp, LAS unsigned char* lds, int wave, int bid, int G) {
;     ...
;     for (int m = bid * NWAVES + wave; m < T; m += G * NWAVES) {
;         const GAS f32x4* xr = (const GAS f32x4*)(X1 + (size_t)m * DM) + lane;
;         const i32x4 te = *(const GAS i32x4*)(TOPI + m * 4), rk = *(const GAS i32x4*)(TRANK + m * 4); const f32x4 tw = *(const GAS f32x4*)(TOPW + m * 4);
;         const i32x4 sl = (i32x4){pstart[te.x] + rk.x, pstart[te.y] + rk.y, pstart[te.z] + rk.z, pstart[te.w] + rk.w};
;         const GAS u32x2* y0 = (const GAS u32x2*)(YS + (size_t)sl.x * DM) + lane; const GAS u32x2* y1 = (const GAS u32x2*)(YS + (size_t)sl.y * DM) + lane;
;         const GAS u32x2* y2 = (const GAS u32x2*)(YS + (size_t)sl.z * DM) + lane; const GAS u32x2* y3 = (const GAS u32x2*)(YS + (size_t)sl.w * DM) + lane;
;         f32x4 v[8]; float s = 0.f;
; #pragma unroll
;         for (int j = 0; j < 8; ++j) {
;             const f32x4 mo = tw.x * unpack4(y0[64 * j]) + tw.y * unpack4(y1[64 * j]) + tw.z * unpack4(y2[64 * j]) + tw.w * unpack4(y3[64 * j]);
;             const f32x4 g2 = *(const GAS f32x4*)(mod + 5 * 2048 + 256 * j + 4 * lane);
;             v[j] = xr[64 * j] + g2 * mo; s += dot4(v[j], v[j]); }
.LBB0_4680:
	s_lshl_b32 s2, s81, 3
	s_add_i32 s2, s82, s2
	s_cmpk_gt_i32 s2, 0x1fff
	s_waitcnt vmcnt(0)
	v_mbcnt_lo_u32_b32 v0, -1, 0
	v_mbcnt_hi_u32_b32 v0, -1, v0
	s_cbranch_scc1 .LBB0_4683
	s_load_dwordx2 s[12:13], s[0:1], 0xc8
	s_load_dwordx4 s[8:11], s[0:1], 0xb8
	s_waitcnt lgkmcnt(0)
	v_mbcnt_lo_u32_b32 v6, -1, 0
	v_ashrrev_i32_e32 v1, 31, v0
	v_mbcnt_hi_u32_b32 v6, -1, v6
	v_lshl_add_u64 v[2:3], v[0:1], 3, s[12:13]
	s_mov_b64 s[0:1], 0x6e000000
	v_and_b32_e32 v7, 64, v6
	v_lshl_add_u64 v[68:69], v[2:3], 0, s[0:1]
	v_lshlrev_b32_e32 v2, 2, v0
	v_add_u32_e32 v7, 64, v7
	v_xor_b32_e32 v8, 1, v6
	v_ashrrev_i32_e32 v3, 31, v2
	v_cmp_lt_i32_e32 vcc, v8, v7
	v_lshlrev_b64 v[2:3], 2, v[2:3]
	v_lshl_add_u64 v[4:5], s[12:13], 0, v[2:3]
	v_cndmask_b32_e32 v8, v6, v8, vcc
	s_mov_b64 s[0:1], 0x20a000
	v_lshlrev_b32_e32 v94, 2, v8
	v_xor_b32_e32 v8, 2, v6
	v_lshl_add_u64 v[70:71], v[4:5], 0, s[0:1]
	v_cmp_lt_i32_e32 vcc, v8, v7
	s_mov_b64 s[0:1], 0x20b000
	v_lshl_add_u64 v[74:75], v[4:5], 0, s[0:1]
	v_cndmask_b32_e32 v8, v6, v8, vcc
	s_mov_b64 s[0:1], 0x20b400
	v_lshlrev_b32_e32 v95, 2, v8
	v_xor_b32_e32 v8, 4, v6
	v_lshl_add_u64 v[76:77], v[4:5], 0, s[0:1]
	s_mov_b64 s[0:1], 0x20b800
	s_add_u32 s14, s12, 0x500000
	v_cmp_lt_i32_e32 vcc, v8, v7
	v_lshl_add_u64 v[78:79], v[4:5], 0, s[0:1]
	s_mov_b64 s[0:1], 0x20bc00
	s_addc_u32 s15, s13, 0
	v_cndmask_b32_e32 v8, v6, v8, vcc
	v_lshl_add_u64 v[72:73], s[8:9], 0, v[2:3]
	v_lshl_add_u64 v[80:81], v[4:5], 0, s[0:1]
	s_mov_b64 s[0:1], 0x1000
	s_add_u32 s17, s12, 0x580000
	v_lshlrev_b32_e32 v96, 2, v8
	v_xor_b32_e32 v8, 8, v6
	v_lshl_add_u64 v[82:83], v[72:73], 0, s[0:1]
	s_mov_b64 s[0:1], 0x1400
	s_addc_u32 s18, s13, 0
	v_cmp_lt_i32_e32 vcc, v8, v7
	v_lshl_add_u64 v[84:85], v[72:73], 0, s[0:1]
	s_mov_b64 s[0:1], 0x1800
	s_add_u32 s19, s12, 0x540000
	v_cndmask_b32_e32 v8, v6, v8, vcc
	v_lshl_add_u64 v[86:87], v[72:73], 0, s[0:1]
	s_mov_b64 s[0:1], 0x1c00
	s_addc_u32 s20, s13, 0
	v_lshlrev_b32_e32 v97, 2, v8
	v_xor_b32_e32 v8, 16, v6
	v_lshl_add_u64 v[88:89], v[72:73], 0, s[0:1]
	s_lshl_b32 s0, s81, 5
	s_lshl_b32 s1, s82, 2
	s_ashr_i32 s3, s2, 31
	s_lshl_b32 s6, s16, 3
	v_cmp_lt_i32_e32 vcc, v8, v7
	s_add_i32 s4, s0, s1
	s_lshl_b32 s16, s16, 5
	s_lshl_b64 s[0:1], s[2:3], 13
	v_cndmask_b32_e32 v8, v6, v8, vcc
	s_add_u32 s8, s10, s0
	v_lshlrev_b32_e32 v98, 2, v8
	v_xor_b32_e32 v8, 32, v6
	s_addc_u32 s9, s11, s1
	s_ashr_i32 s7, s6, 31
	v_cmp_lt_i32_e32 vcc, v8, v7
	s_lshl_b64 s[10:11], s[6:7], 13
	s_add_u32 s12, s12, s0
	v_cndmask_b32_e32 v6, v6, v8, vcc
	v_lshlrev_b32_e32 v99, 2, v6
	v_lshlrev_b64 v[90:91], 4, v[0:1]
	s_addc_u32 s13, s13, s1
	v_mov_b32_e32 v100, 0
	s_add_i32 s3, 0, 0x27000
	s_mov_b32 s7, 0x56000000
	s_mov_b32 s21, 0x56001000
	v_mov_b32_e32 v101, 0x3727c5ac
	s_mov_b32 s22, 0xf800000
	v_mov_b32_e32 v102, 0x260
	s_movk_i32 s23, 0x1000
	s_ashr_i32 s5, s4, 31
	s_lshl_b64 s[0:1], s[4:5], 2
	s_add_u32 s24, s14, s0
	s_addc_u32 s25, s15, s1
	global_load_dwordx4 v[238:241], v100, s[24:25]
	s_add_u32 s24, s17, s0
	s_addc_u32 s25, s18, s1
	global_load_dwordx4 v[242:245], v100, s[24:25]
	v_lshl_add_u64 v[36:37], s[12:13], 0, v[90:91]
	s_ashr_i32 s5, s4, 31
	v_add_co_u32_e32 v104, vcc, s7, v36
	s_lshl_b64 s[0:1], s[4:5], 2
	s_nop 0
	v_addc_co_u32_e32 v105, vcc, 0, v37, vcc
	v_add_co_u32_e32 v106, vcc, s21, v36
	s_nop 0
	v_addc_co_u32_e32 v107, vcc, 0, v37, vcc
	global_load_dwordx4 v[0:3], v[70:71], off nt
	global_load_dwordx4 v[4:7], v[70:71], off offset:1024 nt
	global_load_dwordx4 v[8:11], v[70:71], off offset:2048 nt
	global_load_dwordx4 v[12:15], v[70:71], off offset:3072 nt
	global_load_dwordx4 v[16:19], v[74:75], off nt
	global_load_dwordx4 v[20:23], v[76:77], off nt
	global_load_dwordx4 v[24:27], v[78:79], off nt
	global_load_dwordx4 v[32:35], v[80:81], off nt
	global_load_dwordx4 v[28:31], v[72:73], off
	global_load_dwordx4 v[60:63], v[104:105], off offset:1024
	global_load_dwordx4 v[56:59], v[104:105], off offset:2048
	global_load_dwordx4 v[48:51], v[104:105], off offset:3072
	global_load_dwordx4 v[64:67], v[106:107], off offset:-4096
	global_load_dwordx4 v[52:55], v[106:107], off
	global_load_dwordx4 v[44:47], v[106:107], off offset:1024
	global_load_dwordx4 v[40:43], v[106:107], off offset:2048
	global_load_dwordx4 v[36:39], v[106:107], off offset:3072
	v_lshl_add_u64 v[92:93], s[8:9], 0, v[90:91]
	s_add_u32 s0, s19, s0
	s_addc_u32 s1, s20, s1
	global_load_dwordx4 v[112:115], v100, s[0:1]
	s_waitcnt vmcnt(18)
	s_branch .Lp12_mid
.LBB0_4682:
	v_lshl_add_u64 v[36:37], s[12:13], 0, v[90:91]
	s_ashr_i32 s5, s4, 31
	v_add_co_u32_e32 v104, vcc, s7, v36
	s_lshl_b64 s[0:1], s[4:5], 2
	s_nop 0
	v_addc_co_u32_e32 v105, vcc, 0, v37, vcc
	v_add_co_u32_e32 v106, vcc, s21, v36
	s_nop 0
	v_addc_co_u32_e32 v107, vcc, 0, v37, vcc
	global_load_dwordx4 v[0:3], v[70:71], off nt
	global_load_dwordx4 v[4:7], v[70:71], off offset:1024 nt
	global_load_dwordx4 v[8:11], v[70:71], off offset:2048 nt
	global_load_dwordx4 v[12:15], v[70:71], off offset:3072 nt
	global_load_dwordx4 v[16:19], v[74:75], off nt
	global_load_dwordx4 v[20:23], v[76:77], off nt
	global_load_dwordx4 v[24:27], v[78:79], off nt
	global_load_dwordx4 v[32:35], v[80:81], off nt
	global_load_dwordx4 v[28:31], v[72:73], off
	global_load_dwordx4 v[60:63], v[104:105], off offset:1024
	global_load_dwordx4 v[56:59], v[104:105], off offset:2048
	global_load_dwordx4 v[48:51], v[104:105], off offset:3072
	global_load_dwordx4 v[64:67], v[106:107], off offset:-4096
	global_load_dwordx4 v[52:55], v[106:107], off
	global_load_dwordx4 v[44:47], v[106:107], off offset:1024
	global_load_dwordx4 v[40:43], v[106:107], off offset:2048
	global_load_dwordx4 v[36:39], v[106:107], off offset:3072
	v_lshl_add_u64 v[92:93], s[8:9], 0, v[90:91]
	s_add_u32 s0, s19, s0
	s_addc_u32 s1, s20, s1
	global_load_dwordx4 v[112:115], v100, s[0:1]
